# routing stage 1: the two threads of a list exchange their 16 candidates by DPP instead of an LDS round trip (two workgroup barriers per head pass removed)
# speedup vs baseline: 1.0075x; 1.0075x over previous
; DI void routing_block(LAS unsigned char* lds, const bf16* q, const bf16* skb, int* experts, float* pgates, int tb) {
;     ...
;         const int t0 = tb * 32, hc = 8 * hp + wave;
;         f32x16 acc[4];
; #pragma unroll
;         for (int kb = 0; kb < 4; ++kb)
; #pragma unroll
;             for (int i = 0; i < 16; ++i) acc[kb][i] = 0.f;
; #pragma unroll
;         for (int ks = 0; ks < 8; ++ks) {
;             const bf16x8 a = *(const bf16x8*)(q + (size_t)(t0 + r) * QW + hc * 128 + 16 * ks + 8 * h);
; #pragma unroll
;             for (int kb = 0; kb < 4; ++kb) {
;                 const bf16x8 b = *(const bf16x8*)(skb + ((size_t)hc * 128 + 32 * kb + r) * 128 + 16 * ks + 8 * h);
;                 acc[kb] = __builtin_amdgcn_mfma_f32_32x32x16_bf16(a, b, acc[kb], 0, 0, 0);
;             }
;         }
.LBB0_894:
	s_lshl_b32 s76, s78, 3
	s_add_i32 s76, s76, s79
	s_lshl_b32 vcc_lo, s76, 7
	s_ashr_i32 vcc_hi, vcc_lo, 31
	v_lshl_add_u64 v[110:111], vcc, 1, v[80:81]
	s_ashr_i32 s77, s76, 31
	global_load_dwordx4 v[146:149], v[110:111], off
	global_load_dwordx4 v[150:153], v[110:111], off offset:32
	global_load_dwordx4 v[154:157], v[110:111], off offset:64
	global_load_dwordx4 v[158:161], v[110:111], off offset:96
	global_load_dwordx4 v[162:165], v[110:111], off offset:128
	global_load_dwordx4 v[166:169], v[110:111], off offset:160
	global_load_dwordx4 v[170:173], v[110:111], off offset:192
	global_load_dwordx4 v[174:177], v[110:111], off offset:224
	s_lshl_b64 s[76:77], s[76:77], 15
	v_mov_b32_e32 v105, s77
	v_or_b32_e32 v104, s76, v102
	v_lshl_add_u64 v[112:113], v[82:83], 0, v[104:105]
	v_or_b32_e32 v108, 0x2000, v104
	v_mov_b32_e32 v109, s77
	v_or_b32_e32 v106, 0x4000, v104
	v_mov_b32_e32 v107, s77
	v_or_b32_e32 v104, 0x6000, v104
	v_lshl_add_u64 v[242:243], v[82:83], 0, v[108:109]
	v_lshl_add_u64 v[244:245], v[82:83], 0, v[106:107]
	v_lshl_add_u64 v[246:247], v[82:83], 0, v[104:105]
	global_load_dwordx4 v[178:181], v[112:113], off
	global_load_dwordx4 v[182:185], v[242:243], off
	global_load_dwordx4 v[186:189], v[244:245], off
	global_load_dwordx4 v[190:193], v[246:247], off
	global_load_dwordx4 v[194:197], v[112:113], off offset:32
	global_load_dwordx4 v[198:201], v[242:243], off offset:32
	global_load_dwordx4 v[202:205], v[244:245], off offset:32
	global_load_dwordx4 v[206:209], v[246:247], off offset:32
	global_load_dwordx4 v[210:213], v[112:113], off offset:64
	global_load_dwordx4 v[214:217], v[242:243], off offset:64
	global_load_dwordx4 v[218:221], v[244:245], off offset:64
	global_load_dwordx4 v[222:225], v[246:247], off offset:64
	global_load_dwordx4 v[226:229], v[112:113], off offset:96
	global_load_dwordx4 v[230:233], v[242:243], off offset:96
	global_load_dwordx4 v[234:237], v[244:245], off offset:96
	global_load_dwordx4 v[238:241], v[246:247], off offset:96
	s_xor_b64 s[74:75], s[74:75], -1
	s_mov_b32 s76, 0
	s_waitcnt vmcnt(12)
	v_mfma_f32_32x32x16_bf16 v[50:65], v[146:149], v[178:181], 0
	v_mfma_f32_32x32x16_bf16 v[34:49], v[146:149], v[182:185], 0
	v_mfma_f32_32x32x16_bf16 v[18:33], v[146:149], v[186:189], 0
	v_mfma_f32_32x32x16_bf16 v[2:17], v[146:149], v[190:193], 0
	global_load_dwordx4 v[178:181], v[112:113], off offset:128
	global_load_dwordx4 v[182:185], v[242:243], off offset:128
	global_load_dwordx4 v[186:189], v[244:245], off offset:128
	global_load_dwordx4 v[190:193], v[246:247], off offset:128
	s_waitcnt vmcnt(12)
	v_mfma_f32_32x32x16_bf16 v[50:65], v[150:153], v[194:197], v[50:65]
	v_mfma_f32_32x32x16_bf16 v[34:49], v[150:153], v[198:201], v[34:49]
	v_mfma_f32_32x32x16_bf16 v[18:33], v[150:153], v[202:205], v[18:33]
	v_mfma_f32_32x32x16_bf16 v[2:17], v[150:153], v[206:209], v[2:17]
	global_load_dwordx4 v[194:197], v[112:113], off offset:160
	global_load_dwordx4 v[198:201], v[242:243], off offset:160
	global_load_dwordx4 v[202:205], v[244:245], off offset:160
	global_load_dwordx4 v[206:209], v[246:247], off offset:160
	s_waitcnt vmcnt(12)
	v_mfma_f32_32x32x16_bf16 v[50:65], v[154:157], v[210:213], v[50:65]
	v_mfma_f32_32x32x16_bf16 v[34:49], v[154:157], v[214:217], v[34:49]
	v_mfma_f32_32x32x16_bf16 v[18:33], v[154:157], v[218:221], v[18:33]
	v_mfma_f32_32x32x16_bf16 v[2:17], v[154:157], v[222:225], v[2:17]
	global_load_dwordx4 v[210:213], v[112:113], off offset:192
	global_load_dwordx4 v[214:217], v[242:243], off offset:192
	global_load_dwordx4 v[218:221], v[244:245], off offset:192
	global_load_dwordx4 v[222:225], v[246:247], off offset:192
	s_waitcnt vmcnt(12)
	v_mfma_f32_32x32x16_bf16 v[50:65], v[158:161], v[226:229], v[50:65]
	v_mfma_f32_32x32x16_bf16 v[34:49], v[158:161], v[230:233], v[34:49]
	v_mfma_f32_32x32x16_bf16 v[18:33], v[158:161], v[234:237], v[18:33]
	v_mfma_f32_32x32x16_bf16 v[2:17], v[158:161], v[238:241], v[2:17]
	global_load_dwordx4 v[226:229], v[112:113], off offset:224
	global_load_dwordx4 v[230:233], v[242:243], off offset:224
	global_load_dwordx4 v[234:237], v[244:245], off offset:224
	global_load_dwordx4 v[238:241], v[246:247], off offset:224
	s_waitcnt vmcnt(12)
	v_mfma_f32_32x32x16_bf16 v[50:65], v[162:165], v[178:181], v[50:65]
	v_mfma_f32_32x32x16_bf16 v[34:49], v[162:165], v[182:185], v[34:49]
	v_mfma_f32_32x32x16_bf16 v[18:33], v[162:165], v[186:189], v[18:33]
	v_mfma_f32_32x32x16_bf16 v[2:17], v[162:165], v[190:193], v[2:17]
	s_waitcnt vmcnt(8)
	v_mfma_f32_32x32x16_bf16 v[50:65], v[166:169], v[194:197], v[50:65]
	v_mfma_f32_32x32x16_bf16 v[34:49], v[166:169], v[198:201], v[34:49]
	v_mfma_f32_32x32x16_bf16 v[18:33], v[166:169], v[202:205], v[18:33]
	v_mfma_f32_32x32x16_bf16 v[2:17], v[166:169], v[206:209], v[2:17]
	s_waitcnt vmcnt(4)
	v_mfma_f32_32x32x16_bf16 v[50:65], v[170:173], v[210:213], v[50:65]
	v_mfma_f32_32x32x16_bf16 v[34:49], v[170:173], v[214:217], v[34:49]
	v_mfma_f32_32x32x16_bf16 v[18:33], v[170:173], v[218:221], v[18:33]
	v_mfma_f32_32x32x16_bf16 v[2:17], v[170:173], v[222:225], v[2:17]
	s_waitcnt vmcnt(0)
; DI int crow(int reg, int h) { return (reg & 3) + 8 * (reg >> 2) + 4 * h; }
; DI void routing_block(LAS unsigned char* lds, const bf16* q, const bf16* skb, int* experts, float* pgates, int tb) {
;     ...
;                 acc[kb] = __builtin_amdgcn_mfma_f32_32x32x16_bf16(a, b, acc[kb], 0, 0, 0);
;             }
;         }
; #pragma unroll
;         for (int kb = 0; kb < 4; ++kb)
; #pragma unroll
;             for (int i = 0; i < 16; ++i) {
;                 const int key = 32 * kb + r;
;                 sc[(crow(i, h) * 8 + wave) * RT_PITCH + key] = (f2key(acc[kb][i]) & ~127) | key;
;             }
	v_mfma_f32_32x32x16_bf16 v[50:65], v[174:177], v[226:229], v[50:65]
	v_mfma_f32_32x32x16_bf16 v[34:49], v[174:177], v[230:233], v[34:49]
	v_mfma_f32_32x32x16_bf16 v[18:33], v[174:177], v[234:237], v[18:33]
	v_mfma_f32_32x32x16_bf16 v[2:17], v[174:177], v[238:241], v[2:17]
	s_nop 11
	v_ashrrev_i32_e32 v105, 31, v51
	v_and_b32_e32 v105, 0x7fffff80, v105
	v_and_b32_e32 v51, 0xffffff80, v51
	v_bitop3_b32 v51, v105, v103, v51 bitop3:0xde
	v_ashrrev_i32_e32 v105, 31, v52
	v_and_b32_e32 v105, 0x7fffff80, v105
	v_and_b32_e32 v52, 0xffffff80, v52
	v_bitop3_b32 v52, v105, v103, v52 bitop3:0xde
	v_ashrrev_i32_e32 v105, 31, v53
	v_and_b32_e32 v105, 0x7fffff80, v105
	v_and_b32_e32 v53, 0xffffff80, v53
	v_bitop3_b32 v53, v105, v103, v53 bitop3:0xde
	v_ashrrev_i32_e32 v105, 31, v54
	v_and_b32_e32 v105, 0x7fffff80, v105
	v_and_b32_e32 v54, 0xffffff80, v54
	v_bitop3_b32 v54, v105, v103, v54 bitop3:0xde
	v_ashrrev_i32_e32 v105, 31, v55
	v_and_b32_e32 v105, 0x7fffff80, v105
	v_and_b32_e32 v55, 0xffffff80, v55
	v_bitop3_b32 v55, v105, v103, v55 bitop3:0xde
	v_ashrrev_i32_e32 v105, 31, v56
	v_and_b32_e32 v105, 0x7fffff80, v105
	v_and_b32_e32 v56, 0xffffff80, v56
	v_bitop3_b32 v56, v105, v103, v56 bitop3:0xde
	v_ashrrev_i32_e32 v105, 31, v57
	v_and_b32_e32 v105, 0x7fffff80, v105
	v_and_b32_e32 v57, 0xffffff80, v57
	v_bitop3_b32 v57, v105, v103, v57 bitop3:0xde
	v_ashrrev_i32_e32 v105, 31, v58
	v_and_b32_e32 v105, 0x7fffff80, v105
	v_and_b32_e32 v58, 0xffffff80, v58
	v_bitop3_b32 v58, v105, v103, v58 bitop3:0xde
	v_ashrrev_i32_e32 v105, 31, v59
	v_and_b32_e32 v105, 0x7fffff80, v105
	v_and_b32_e32 v59, 0xffffff80, v59
	v_bitop3_b32 v59, v105, v103, v59 bitop3:0xde
	v_ashrrev_i32_e32 v105, 31, v60
	v_and_b32_e32 v105, 0x7fffff80, v105
	v_and_b32_e32 v60, 0xffffff80, v60
	v_bitop3_b32 v60, v105, v103, v60 bitop3:0xde
	v_ashrrev_i32_e32 v105, 31, v61
	v_and_b32_e32 v105, 0x7fffff80, v105
	v_and_b32_e32 v61, 0xffffff80, v61
	v_bitop3_b32 v61, v105, v103, v61 bitop3:0xde
	v_ashrrev_i32_e32 v105, 31, v62
	v_and_b32_e32 v105, 0x7fffff80, v105
	v_and_b32_e32 v62, 0xffffff80, v62
	v_bitop3_b32 v62, v105, v103, v62 bitop3:0xde
	v_ashrrev_i32_e32 v105, 31, v63
	v_and_b32_e32 v105, 0x7fffff80, v105
	v_and_b32_e32 v63, 0xffffff80, v63
	v_bitop3_b32 v63, v105, v103, v63 bitop3:0xde
	v_ashrrev_i32_e32 v105, 31, v64
	v_and_b32_e32 v105, 0x7fffff80, v105
	v_and_b32_e32 v64, 0xffffff80, v64
	v_bitop3_b32 v64, v105, v103, v64 bitop3:0xde
	v_ashrrev_i32_e32 v105, 31, v65
	v_and_b32_e32 v105, 0x7fffff80, v105
	v_and_b32_e32 v65, 0xffffff80, v65
	v_ashrrev_i32_e32 v104, 31, v50
	v_bitop3_b32 v65, v105, v103, v65 bitop3:0xde
	v_ashrrev_i32_e32 v105, 31, v34
	v_and_b32_e32 v104, 0x7fffff80, v104
	v_and_b32_e32 v50, 0xffffff80, v50
	v_and_b32_e32 v105, 0x7fffff80, v105
	v_and_b32_e32 v34, 0xffffff80, v34
	v_bitop3_b32 v50, v104, v103, v50 bitop3:0xde
	v_add_u32_e32 v104, v123, v124
	v_bitop3_b32 v34, v105, v125, v34 bitop3:0xde
	ds_write2_b32 v104, v50, v34 offset1:32
	v_ashrrev_i32_e32 v34, 31, v35
	v_and_b32_e32 v34, 0x7fffff80, v34
	v_and_b32_e32 v35, 0xffffff80, v35
	v_bitop3_b32 v34, v34, v125, v35 bitop3:0xde
	v_add_u32_e32 v35, 0x1000, v104
	ds_write2_b32 v35, v51, v34 offset0:8 offset1:40
	v_ashrrev_i32_e32 v34, 31, v36
	v_and_b32_e32 v34, 0x7fffff80, v34
	v_and_b32_e32 v36, 0xffffff80, v36
	v_bitop3_b32 v34, v34, v125, v36 bitop3:0xde
	v_add_u32_e32 v36, 0x2000, v104
	ds_write2_b32 v36, v52, v34 offset0:16 offset1:48
	v_ashrrev_i32_e32 v34, 31, v37
	v_and_b32_e32 v34, 0x7fffff80, v34
	v_and_b32_e32 v37, 0xffffff80, v37
	v_bitop3_b32 v34, v34, v125, v37 bitop3:0xde
	v_add_u32_e32 v37, 0x3000, v104
	ds_write2_b32 v37, v53, v34 offset0:24 offset1:56
	v_ashrrev_i32_e32 v34, 31, v38
	v_and_b32_e32 v34, 0x7fffff80, v34
	v_and_b32_e32 v38, 0xffffff80, v38
	v_bitop3_b32 v34, v34, v125, v38 bitop3:0xde
	v_add_u32_e32 v38, 0x8000, v104
	ds_write2_b32 v38, v54, v34 offset0:64 offset1:96
	v_ashrrev_i32_e32 v34, 31, v39
	v_and_b32_e32 v34, 0x7fffff80, v34
	v_and_b32_e32 v39, 0xffffff80, v39
	v_bitop3_b32 v34, v34, v125, v39 bitop3:0xde
	v_add_u32_e32 v39, 0x9000, v104
	ds_write2_b32 v39, v55, v34 offset0:72 offset1:104
	v_ashrrev_i32_e32 v34, 31, v40
	v_and_b32_e32 v34, 0x7fffff80, v34
	v_and_b32_e32 v40, 0xffffff80, v40
	v_bitop3_b32 v34, v34, v125, v40 bitop3:0xde
	v_add_u32_e32 v40, 0xa000, v104
	ds_write2_b32 v40, v56, v34 offset0:80 offset1:112
	v_ashrrev_i32_e32 v34, 31, v41
	v_and_b32_e32 v34, 0x7fffff80, v34
	v_and_b32_e32 v41, 0xffffff80, v41
	v_bitop3_b32 v34, v34, v125, v41 bitop3:0xde
	v_add_u32_e32 v41, 0xb000, v104
	ds_write2_b32 v41, v57, v34 offset0:88 offset1:120
	v_ashrrev_i32_e32 v34, 31, v42
	v_and_b32_e32 v34, 0x7fffff80, v34
	v_and_b32_e32 v42, 0xffffff80, v42
	v_bitop3_b32 v34, v34, v125, v42 bitop3:0xde
	ds_write2_b32 v128, v58, v34 offset1:32
	v_ashrrev_i32_e32 v34, 31, v43
	v_and_b32_e32 v34, 0x7fffff80, v34
	v_and_b32_e32 v42, 0xffffff80, v43
	v_bitop3_b32 v34, v34, v125, v42 bitop3:0xde
	ds_write2_b32 v129, v59, v34 offset1:32
	v_ashrrev_i32_e32 v34, 31, v44
	v_and_b32_e32 v34, 0x7fffff80, v34
	v_and_b32_e32 v42, 0xffffff80, v44
	v_bitop3_b32 v34, v34, v125, v42 bitop3:0xde
	ds_write2_b32 v130, v60, v34 offset1:32
	v_ashrrev_i32_e32 v34, 31, v45
	v_and_b32_e32 v34, 0x7fffff80, v34
	v_and_b32_e32 v42, 0xffffff80, v45
	v_bitop3_b32 v34, v34, v125, v42 bitop3:0xde
	ds_write2_b32 v131, v61, v34 offset1:32
	v_ashrrev_i32_e32 v34, 31, v46
	v_and_b32_e32 v34, 0x7fffff80, v34
	v_and_b32_e32 v42, 0xffffff80, v46
	v_bitop3_b32 v34, v34, v125, v42 bitop3:0xde
	ds_write2_b32 v132, v62, v34 offset1:32
	v_ashrrev_i32_e32 v34, 31, v47
	v_and_b32_e32 v34, 0x7fffff80, v34
; DI int crow(int reg, int h) { return (reg & 3) + 8 * (reg >> 2) + 4 * h; }
; DI void routing_block(LAS unsigned char* lds, const bf16* q, const bf16* skb, int* experts, float* pgates, int tb) {
;     ...
; #pragma unroll
;         for (int kb = 0; kb < 4; ++kb)
; #pragma unroll
;             for (int i = 0; i < 16; ++i) {
;                 const int key = 32 * kb + r;
;                 sc[(crow(i, h) * 8 + wave) * RT_PITCH + key] = (f2key(acc[kb][i]) & ~127) | key;
;             }
;         __syncthreads();
	v_and_b32_e32 v42, 0xffffff80, v47
	v_bitop3_b32 v34, v34, v125, v42 bitop3:0xde
	ds_write2_b32 v133, v63, v34 offset1:32
	v_ashrrev_i32_e32 v34, 31, v48
	v_and_b32_e32 v34, 0x7fffff80, v34
	v_and_b32_e32 v42, 0xffffff80, v48
	v_bitop3_b32 v34, v34, v125, v42 bitop3:0xde
	ds_write2_b32 v134, v64, v34 offset1:32
	v_ashrrev_i32_e32 v34, 31, v49
	v_and_b32_e32 v34, 0x7fffff80, v34
	v_and_b32_e32 v42, 0xffffff80, v49
	v_bitop3_b32 v34, v34, v125, v42 bitop3:0xde
	ds_write2_b32 v135, v65, v34 offset1:32
	v_ashrrev_i32_e32 v34, 31, v18
	v_and_b32_e32 v34, 0x7fffff80, v34
	v_and_b32_e32 v18, 0xffffff80, v18
	v_bitop3_b32 v18, v34, v126, v18 bitop3:0xde
	v_ashrrev_i32_e32 v34, 31, v19
	v_and_b32_e32 v34, 0x7fffff80, v34
	v_and_b32_e32 v19, 0xffffff80, v19
	v_bitop3_b32 v19, v34, v126, v19 bitop3:0xde
	v_ashrrev_i32_e32 v34, 31, v20
	v_and_b32_e32 v34, 0x7fffff80, v34
	v_and_b32_e32 v20, 0xffffff80, v20
	v_bitop3_b32 v20, v34, v126, v20 bitop3:0xde
	v_ashrrev_i32_e32 v34, 31, v21
	v_and_b32_e32 v34, 0x7fffff80, v34
	v_and_b32_e32 v21, 0xffffff80, v21
	v_bitop3_b32 v21, v34, v126, v21 bitop3:0xde
	v_ashrrev_i32_e32 v34, 31, v22
	v_and_b32_e32 v34, 0x7fffff80, v34
	v_and_b32_e32 v22, 0xffffff80, v22
	v_bitop3_b32 v22, v34, v126, v22 bitop3:0xde
	v_ashrrev_i32_e32 v34, 31, v23
	v_and_b32_e32 v34, 0x7fffff80, v34
	v_and_b32_e32 v23, 0xffffff80, v23
	v_bitop3_b32 v23, v34, v126, v23 bitop3:0xde
	v_ashrrev_i32_e32 v34, 31, v24
	v_and_b32_e32 v34, 0x7fffff80, v34
	v_and_b32_e32 v24, 0xffffff80, v24
	v_bitop3_b32 v24, v34, v126, v24 bitop3:0xde
	v_ashrrev_i32_e32 v34, 31, v25
	v_and_b32_e32 v34, 0x7fffff80, v34
	v_and_b32_e32 v25, 0xffffff80, v25
	v_bitop3_b32 v25, v34, v126, v25 bitop3:0xde
	v_ashrrev_i32_e32 v34, 31, v26
	v_and_b32_e32 v34, 0x7fffff80, v34
	v_and_b32_e32 v26, 0xffffff80, v26
	v_bitop3_b32 v26, v34, v126, v26 bitop3:0xde
	v_ashrrev_i32_e32 v34, 31, v27
	v_and_b32_e32 v34, 0x7fffff80, v34
	v_and_b32_e32 v27, 0xffffff80, v27
	v_bitop3_b32 v27, v34, v126, v27 bitop3:0xde
	v_ashrrev_i32_e32 v34, 31, v28
	v_and_b32_e32 v34, 0x7fffff80, v34
	v_and_b32_e32 v28, 0xffffff80, v28
	v_bitop3_b32 v28, v34, v126, v28 bitop3:0xde
	v_ashrrev_i32_e32 v34, 31, v29
	v_and_b32_e32 v34, 0x7fffff80, v34
	v_and_b32_e32 v29, 0xffffff80, v29
	v_bitop3_b32 v29, v34, v126, v29 bitop3:0xde
	v_ashrrev_i32_e32 v34, 31, v30
	v_and_b32_e32 v34, 0x7fffff80, v34
	v_and_b32_e32 v30, 0xffffff80, v30
	v_bitop3_b32 v30, v34, v126, v30 bitop3:0xde
	v_ashrrev_i32_e32 v34, 31, v31
	v_and_b32_e32 v34, 0x7fffff80, v34
	v_and_b32_e32 v31, 0xffffff80, v31
	v_bitop3_b32 v31, v34, v126, v31 bitop3:0xde
	v_ashrrev_i32_e32 v34, 31, v32
	v_and_b32_e32 v34, 0x7fffff80, v34
	v_and_b32_e32 v32, 0xffffff80, v32
	v_bitop3_b32 v32, v34, v126, v32 bitop3:0xde
	v_ashrrev_i32_e32 v34, 31, v33
	v_and_b32_e32 v34, 0x7fffff80, v34
	v_and_b32_e32 v33, 0xffffff80, v33
	v_bitop3_b32 v33, v34, v126, v33 bitop3:0xde
	v_ashrrev_i32_e32 v34, 31, v2
	v_and_b32_e32 v34, 0x7fffff80, v34
	v_and_b32_e32 v2, 0xffffff80, v2
	v_bitop3_b32 v2, v34, v127, v2 bitop3:0xde
	ds_write2_b32 v104, v18, v2 offset0:64 offset1:96
	v_ashrrev_i32_e32 v2, 31, v3
	v_and_b32_e32 v2, 0x7fffff80, v2
	v_and_b32_e32 v3, 0xffffff80, v3
	v_bitop3_b32 v2, v2, v127, v3 bitop3:0xde
	ds_write2_b32 v35, v19, v2 offset0:72 offset1:104
	v_ashrrev_i32_e32 v2, 31, v4
	v_and_b32_e32 v2, 0x7fffff80, v2
	v_and_b32_e32 v3, 0xffffff80, v4
	v_bitop3_b32 v2, v2, v127, v3 bitop3:0xde
	ds_write2_b32 v36, v20, v2 offset0:80 offset1:112
	v_ashrrev_i32_e32 v2, 31, v5
	v_and_b32_e32 v2, 0x7fffff80, v2
	v_and_b32_e32 v3, 0xffffff80, v5
	v_bitop3_b32 v2, v2, v127, v3 bitop3:0xde
	ds_write2_b32 v37, v21, v2 offset0:88 offset1:120
	v_ashrrev_i32_e32 v2, 31, v6
	v_and_b32_e32 v2, 0x7fffff80, v2
	v_and_b32_e32 v3, 0xffffff80, v6
	v_bitop3_b32 v2, v2, v127, v3 bitop3:0xde
	ds_write2_b32 v38, v22, v2 offset0:128 offset1:160
	v_ashrrev_i32_e32 v2, 31, v7
	v_and_b32_e32 v2, 0x7fffff80, v2
	v_and_b32_e32 v3, 0xffffff80, v7
	v_bitop3_b32 v2, v2, v127, v3 bitop3:0xde
	ds_write2_b32 v39, v23, v2 offset0:136 offset1:168
	v_ashrrev_i32_e32 v2, 31, v8
	v_and_b32_e32 v2, 0x7fffff80, v2
	v_and_b32_e32 v3, 0xffffff80, v8
	v_bitop3_b32 v2, v2, v127, v3 bitop3:0xde
	ds_write2_b32 v40, v24, v2 offset0:144 offset1:176
	v_ashrrev_i32_e32 v2, 31, v9
	v_and_b32_e32 v2, 0x7fffff80, v2
	v_and_b32_e32 v3, 0xffffff80, v9
	v_bitop3_b32 v2, v2, v127, v3 bitop3:0xde
	ds_write2_b32 v41, v25, v2 offset0:152 offset1:184
	v_ashrrev_i32_e32 v2, 31, v10
	v_and_b32_e32 v2, 0x7fffff80, v2
	v_and_b32_e32 v3, 0xffffff80, v10
	v_bitop3_b32 v2, v2, v127, v3 bitop3:0xde
	ds_write2_b32 v128, v26, v2 offset0:64 offset1:96
	v_ashrrev_i32_e32 v2, 31, v11
	v_and_b32_e32 v2, 0x7fffff80, v2
	v_and_b32_e32 v3, 0xffffff80, v11
	v_bitop3_b32 v2, v2, v127, v3 bitop3:0xde
	ds_write2_b32 v129, v27, v2 offset0:64 offset1:96
	v_ashrrev_i32_e32 v2, 31, v12
	v_and_b32_e32 v2, 0x7fffff80, v2
	v_and_b32_e32 v3, 0xffffff80, v12
	v_bitop3_b32 v2, v2, v127, v3 bitop3:0xde
	ds_write2_b32 v130, v28, v2 offset0:64 offset1:96
	v_ashrrev_i32_e32 v2, 31, v13
	v_and_b32_e32 v2, 0x7fffff80, v2
	v_and_b32_e32 v3, 0xffffff80, v13
	v_bitop3_b32 v2, v2, v127, v3 bitop3:0xde
	ds_write2_b32 v131, v29, v2 offset0:64 offset1:96
	v_ashrrev_i32_e32 v2, 31, v14
	v_and_b32_e32 v2, 0x7fffff80, v2
	v_and_b32_e32 v3, 0xffffff80, v14
	v_bitop3_b32 v2, v2, v127, v3 bitop3:0xde
	ds_write2_b32 v132, v30, v2 offset0:64 offset1:96
	v_ashrrev_i32_e32 v2, 31, v15
	v_and_b32_e32 v2, 0x7fffff80, v2
	v_and_b32_e32 v3, 0xffffff80, v15
	v_bitop3_b32 v2, v2, v127, v3 bitop3:0xde
	ds_write2_b32 v133, v31, v2 offset0:64 offset1:96
	v_ashrrev_i32_e32 v2, 31, v16
	v_and_b32_e32 v2, 0x7fffff80, v2
	v_and_b32_e32 v3, 0xffffff80, v16
	v_bitop3_b32 v2, v2, v127, v3 bitop3:0xde
	ds_write2_b32 v134, v32, v2 offset0:64 offset1:96
	v_ashrrev_i32_e32 v2, 31, v17
	v_and_b32_e32 v2, 0x7fffff80, v2
	v_and_b32_e32 v3, 0xffffff80, v17
	v_bitop3_b32 v2, v2, v127, v3 bitop3:0xde
	ds_write2_b32 v135, v33, v2 offset0:64 offset1:96
	s_waitcnt lgkmcnt(0)
	s_barrier
; #define LAS __attribute__((address_space(3)))
; #define TOPK_INSERT(arr, xx) do { int _x = (xx); _Pragma("unroll") for (int _j = 0; _j < 16; ++_j) { const int _hi = max(arr[_j], _x); _x = min(arr[_j], _x); arr[_j] = _hi; } } while (0)
; DI void routing_block(LAS unsigned char* lds, const bf16* q, const bf16* skb, int* experts, float* pgates, int tb) {
;     ...
;             int a[16];
; #pragma unroll
;             for (int j = 0; j < 16; ++j) a[j] = (int)0x80000000;
;             LAS int* row = sc + (tid >> 1) * RT_PITCH; const int hf = tid & 1;
; #pragma unroll 8
;             for (int k = 0; k < 64; ++k) { const int x = row[64 * hf + k]; TOPK_INSERT(a, x); }
	ds_read2_b32 v[146:147], v120 offset0:0 offset1:1
	ds_read2_b32 v[148:149], v120 offset0:2 offset1:3
	ds_read2_b32 v[150:151], v120 offset0:4 offset1:5
	ds_read2_b32 v[152:153], v120 offset0:6 offset1:7
	ds_read2_b32 v[154:155], v120 offset0:8 offset1:9
	ds_read2_b32 v[156:157], v120 offset0:10 offset1:11
	ds_read2_b32 v[158:159], v120 offset0:12 offset1:13
	ds_read2_b32 v[160:161], v120 offset0:14 offset1:15
	ds_read2_b32 v[162:163], v120 offset0:16 offset1:17
	ds_read2_b32 v[164:165], v120 offset0:18 offset1:19
	ds_read2_b32 v[166:167], v120 offset0:20 offset1:21
	ds_read2_b32 v[168:169], v120 offset0:22 offset1:23
	ds_read2_b32 v[170:171], v120 offset0:24 offset1:25
	ds_read2_b32 v[172:173], v120 offset0:26 offset1:27
	ds_read2_b32 v[174:175], v120 offset0:28 offset1:29
	ds_read2_b32 v[176:177], v120 offset0:30 offset1:31
	ds_read2_b32 v[178:179], v120 offset0:32 offset1:33
	ds_read2_b32 v[180:181], v120 offset0:34 offset1:35
	ds_read2_b32 v[182:183], v120 offset0:36 offset1:37
	ds_read2_b32 v[184:185], v120 offset0:38 offset1:39
	ds_read2_b32 v[186:187], v120 offset0:40 offset1:41
	ds_read2_b32 v[188:189], v120 offset0:42 offset1:43
	ds_read2_b32 v[190:191], v120 offset0:44 offset1:45
	ds_read2_b32 v[192:193], v120 offset0:46 offset1:47
	ds_read2_b32 v[194:195], v120 offset0:48 offset1:49
	ds_read2_b32 v[196:197], v120 offset0:50 offset1:51
	ds_read2_b32 v[198:199], v120 offset0:52 offset1:53
	ds_read2_b32 v[200:201], v120 offset0:54 offset1:55
	ds_read2_b32 v[202:203], v120 offset0:56 offset1:57
	ds_read2_b32 v[204:205], v120 offset0:58 offset1:59
	ds_read2_b32 v[206:207], v120 offset0:60 offset1:61
	ds_read2_b32 v[208:209], v120 offset0:62 offset1:63
	s_waitcnt lgkmcnt(0)
	v_max_i32_e32 v18, v146, v147
	v_min_i32_e32 v147, v146, v147
	v_max_i32_e32 v19, v148, v149
	v_min_i32_e32 v149, v148, v149
	v_max_i32_e32 v20, v18, v19
	v_min_i32_e32 v19, v18, v19
	v_max_i32_e32 v21, v147, v149
	v_min_i32_e32 v149, v147, v149
	v_max_i32_e32 v146, v21, v19
	v_min_i32_e32 v19, v21, v19
	v_max_i32_e32 v148, v150, v151
	v_min_i32_e32 v151, v150, v151
	v_max_i32_e32 v18, v152, v153
	v_min_i32_e32 v153, v152, v153
	v_max_i32_e32 v147, v148, v18
	v_min_i32_e32 v18, v148, v18
	v_max_i32_e32 v21, v151, v153
	v_min_i32_e32 v153, v151, v153
	v_max_i32_e32 v150, v21, v18
	v_min_i32_e32 v18, v21, v18
	v_max_i32_e32 v152, v20, v147
	v_min_i32_e32 v147, v20, v147
	v_max_i32_e32 v148, v19, v18
	v_min_i32_e32 v18, v19, v18
	v_max_i32_e32 v151, v148, v147
	v_min_i32_e32 v147, v148, v147
	v_max_i32_e32 v21, v146, v150
	v_min_i32_e32 v150, v146, v150
	v_max_i32_e32 v20, v149, v153
	v_min_i32_e32 v153, v149, v153
	v_max_i32_e32 v19, v20, v150
	v_min_i32_e32 v150, v20, v150
	v_max_i32_e32 v148, v21, v151
	v_min_i32_e32 v151, v21, v151
	v_max_i32_e32 v146, v19, v147
	v_min_i32_e32 v147, v19, v147
	v_max_i32_e32 v149, v150, v18
	v_min_i32_e32 v18, v150, v18
	v_max_i32_e32 v20, v154, v155
	v_min_i32_e32 v155, v154, v155
	v_max_i32_e32 v21, v156, v157
	v_min_i32_e32 v157, v156, v157
	v_max_i32_e32 v19, v20, v21
	v_min_i32_e32 v21, v20, v21
	v_max_i32_e32 v150, v155, v157
	v_min_i32_e32 v157, v155, v157
	v_max_i32_e32 v154, v150, v21
	v_min_i32_e32 v21, v150, v21
	v_max_i32_e32 v156, v158, v159
	v_min_i32_e32 v159, v158, v159
	v_max_i32_e32 v20, v160, v161
	v_min_i32_e32 v161, v160, v161
	v_max_i32_e32 v155, v156, v20
	v_min_i32_e32 v20, v156, v20
	v_max_i32_e32 v150, v159, v161
	v_min_i32_e32 v161, v159, v161
	v_max_i32_e32 v158, v150, v20
	v_min_i32_e32 v20, v150, v20
	v_max_i32_e32 v160, v19, v155
	v_min_i32_e32 v155, v19, v155
	v_max_i32_e32 v156, v21, v20
	v_min_i32_e32 v20, v21, v20
	v_max_i32_e32 v159, v156, v155
	v_min_i32_e32 v155, v156, v155
	v_max_i32_e32 v150, v154, v158
	v_min_i32_e32 v158, v154, v158
	v_max_i32_e32 v19, v157, v161
	v_min_i32_e32 v161, v157, v161
	v_max_i32_e32 v21, v19, v158
	v_min_i32_e32 v158, v19, v158
	v_max_i32_e32 v156, v150, v159
	v_min_i32_e32 v159, v150, v159
	v_max_i32_e32 v154, v21, v155
	v_min_i32_e32 v155, v21, v155
	v_max_i32_e32 v157, v158, v20
	v_min_i32_e32 v20, v158, v20
	v_max_i32_e32 v19, v152, v160
	v_min_i32_e32 v160, v152, v160
	v_max_i32_e32 v150, v147, v155
	v_min_i32_e32 v155, v147, v155
	v_max_i32_e32 v21, v150, v160
	v_min_i32_e32 v160, v150, v160
	v_max_i32_e32 v158, v151, v159
	v_min_i32_e32 v159, v151, v159
	v_max_i32_e32 v152, v18, v20
	v_min_i32_e32 v20, v18, v20
	v_max_i32_e32 v147, v152, v159
	v_min_i32_e32 v159, v152, v159
	v_max_i32_e32 v150, v158, v21
	v_min_i32_e32 v21, v158, v21
	v_max_i32_e32 v151, v147, v160
	v_min_i32_e32 v160, v147, v160
	v_max_i32_e32 v18, v159, v155
	v_min_i32_e32 v155, v159, v155
	v_max_i32_e32 v152, v148, v156
	v_min_i32_e32 v156, v148, v156
	v_max_i32_e32 v158, v149, v157
	v_min_i32_e32 v157, v149, v157
	v_max_i32_e32 v147, v158, v156
	v_min_i32_e32 v156, v158, v156
	v_max_i32_e32 v159, v146, v154
	v_min_i32_e32 v154, v146, v154
	v_max_i32_e32 v148, v153, v161
	v_min_i32_e32 v161, v153, v161
	v_max_i32_e32 v149, v148, v154
	v_min_i32_e32 v154, v148, v154
	v_max_i32_e32 v158, v159, v147
	v_min_i32_e32 v147, v159, v147
	v_max_i32_e32 v146, v149, v156
	v_min_i32_e32 v156, v149, v156
	v_max_i32_e32 v153, v154, v157
	v_min_i32_e32 v157, v154, v157
	v_max_i32_e32 v148, v152, v150
	v_min_i32_e32 v150, v152, v150
	v_max_i32_e32 v159, v158, v21
	v_min_i32_e32 v21, v158, v21
	v_max_i32_e32 v149, v147, v151
	v_min_i32_e32 v151, v147, v151
	v_max_i32_e32 v154, v146, v160
	v_min_i32_e32 v160, v146, v160
	v_max_i32_e32 v152, v156, v18
	v_min_i32_e32 v18, v156, v18
	v_max_i32_e32 v158, v153, v155
	v_min_i32_e32 v155, v153, v155
	v_max_i32_e32 v147, v157, v20
	v_min_i32_e32 v20, v157, v20
; #define LAS __attribute__((address_space(3)))
; #define TOPK_INSERT(arr, xx) do { int _x = (xx); _Pragma("unroll") for (int _j = 0; _j < 16; ++_j) { const int _hi = max(arr[_j], _x); _x = min(arr[_j], _x); arr[_j] = _hi; } } while (0)
; DI void routing_block(LAS unsigned char* lds, const bf16* q, const bf16* skb, int* experts, float* pgates, int tb) {
;     ...
;             LAS int* row = sc + (tid >> 1) * RT_PITCH; const int hf = tid & 1;
; #pragma unroll 8
;             for (int k = 0; k < 64; ++k) { const int x = row[64 * hf + k]; TOPK_INSERT(a, x); }
	v_max_i32_e32 v146, v162, v163
	v_min_i32_e32 v163, v162, v163
	v_max_i32_e32 v156, v164, v165
	v_min_i32_e32 v165, v164, v165
	v_max_i32_e32 v153, v146, v156
	v_min_i32_e32 v156, v146, v156
	v_max_i32_e32 v157, v163, v165
	v_min_i32_e32 v165, v163, v165
	v_max_i32_e32 v162, v157, v156
	v_min_i32_e32 v156, v157, v156
	v_max_i32_e32 v164, v166, v167
	v_min_i32_e32 v167, v166, v167
	v_max_i32_e32 v146, v168, v169
	v_min_i32_e32 v169, v168, v169
	v_max_i32_e32 v163, v164, v146
	v_min_i32_e32 v146, v164, v146
	v_max_i32_e32 v157, v167, v169
	v_min_i32_e32 v169, v167, v169
	v_max_i32_e32 v166, v157, v146
	v_min_i32_e32 v146, v157, v146
	v_max_i32_e32 v168, v153, v163
	v_min_i32_e32 v163, v153, v163
	v_max_i32_e32 v164, v156, v146
	v_min_i32_e32 v146, v156, v146
	v_max_i32_e32 v167, v164, v163
	v_min_i32_e32 v163, v164, v163
	v_max_i32_e32 v157, v162, v166
	v_min_i32_e32 v166, v162, v166
	v_max_i32_e32 v153, v165, v169
	v_min_i32_e32 v169, v165, v169
	v_max_i32_e32 v156, v153, v166
	v_min_i32_e32 v166, v153, v166
	v_max_i32_e32 v164, v157, v167
	v_min_i32_e32 v167, v157, v167
	v_max_i32_e32 v162, v156, v163
	v_min_i32_e32 v163, v156, v163
	v_max_i32_e32 v165, v166, v146
	v_min_i32_e32 v146, v166, v146
	v_max_i32_e32 v153, v170, v171
	v_min_i32_e32 v171, v170, v171
	v_max_i32_e32 v157, v172, v173
	v_min_i32_e32 v173, v172, v173
	v_max_i32_e32 v156, v153, v157
	v_min_i32_e32 v157, v153, v157
	v_max_i32_e32 v166, v171, v173
	v_min_i32_e32 v173, v171, v173
	v_max_i32_e32 v170, v166, v157
	v_min_i32_e32 v157, v166, v157
	v_max_i32_e32 v172, v174, v175
	v_min_i32_e32 v175, v174, v175
	v_max_i32_e32 v153, v176, v177
	v_min_i32_e32 v177, v176, v177
	v_max_i32_e32 v171, v172, v153
	v_min_i32_e32 v153, v172, v153
	v_max_i32_e32 v166, v175, v177
	v_min_i32_e32 v177, v175, v177
	v_max_i32_e32 v174, v166, v153
	v_min_i32_e32 v153, v166, v153
	v_max_i32_e32 v176, v156, v171
	v_min_i32_e32 v171, v156, v171
	v_max_i32_e32 v172, v157, v153
	v_min_i32_e32 v153, v157, v153
	v_max_i32_e32 v175, v172, v171
	v_min_i32_e32 v171, v172, v171
	v_max_i32_e32 v166, v170, v174
	v_min_i32_e32 v174, v170, v174
	v_max_i32_e32 v156, v173, v177
	v_min_i32_e32 v177, v173, v177
	v_max_i32_e32 v157, v156, v174
	v_min_i32_e32 v174, v156, v174
	v_max_i32_e32 v172, v166, v175
	v_min_i32_e32 v175, v166, v175
	v_max_i32_e32 v170, v157, v171
	v_min_i32_e32 v171, v157, v171
	v_max_i32_e32 v173, v174, v153
	v_min_i32_e32 v153, v174, v153
	v_max_i32_e32 v156, v168, v176
	v_min_i32_e32 v176, v168, v176
	v_max_i32_e32 v166, v163, v171
	v_min_i32_e32 v171, v163, v171
	v_max_i32_e32 v157, v166, v176
	v_min_i32_e32 v176, v166, v176
	v_max_i32_e32 v174, v167, v175
	v_min_i32_e32 v175, v167, v175
	v_max_i32_e32 v168, v146, v153
	v_min_i32_e32 v153, v146, v153
	v_max_i32_e32 v163, v168, v175
	v_min_i32_e32 v175, v168, v175
	v_max_i32_e32 v166, v174, v157
	v_min_i32_e32 v157, v174, v157
	v_max_i32_e32 v167, v163, v176
	v_min_i32_e32 v176, v163, v176
	v_max_i32_e32 v146, v175, v171
	v_min_i32_e32 v171, v175, v171
	v_max_i32_e32 v168, v164, v172
	v_min_i32_e32 v172, v164, v172
	v_max_i32_e32 v174, v165, v173
	v_min_i32_e32 v173, v165, v173
	v_max_i32_e32 v163, v174, v172
	v_min_i32_e32 v172, v174, v172
	v_max_i32_e32 v175, v162, v170
	v_min_i32_e32 v170, v162, v170
	v_max_i32_e32 v164, v169, v177
	v_min_i32_e32 v177, v169, v177
	v_max_i32_e32 v165, v164, v170
	v_min_i32_e32 v170, v164, v170
	v_max_i32_e32 v174, v175, v163
	v_min_i32_e32 v163, v175, v163
	v_max_i32_e32 v162, v165, v172
	v_min_i32_e32 v172, v165, v172
	v_max_i32_e32 v169, v170, v173
	v_min_i32_e32 v173, v170, v173
	v_max_i32_e32 v164, v168, v166
	v_min_i32_e32 v166, v168, v166
	v_max_i32_e32 v175, v174, v157
	v_min_i32_e32 v157, v174, v157
	v_max_i32_e32 v165, v163, v167
	v_min_i32_e32 v167, v163, v167
	v_max_i32_e32 v170, v162, v176
	v_min_i32_e32 v176, v162, v176
	v_max_i32_e32 v168, v172, v146
	v_min_i32_e32 v146, v172, v146
	v_max_i32_e32 v174, v169, v171
	v_min_i32_e32 v171, v169, v171
	v_max_i32_e32 v163, v173, v153
	v_min_i32_e32 v153, v173, v153
	v_max_i32_e32 v162, v178, v179
	v_min_i32_e32 v179, v178, v179
	v_max_i32_e32 v172, v180, v181
	v_min_i32_e32 v181, v180, v181
	v_max_i32_e32 v169, v162, v172
	v_min_i32_e32 v172, v162, v172
	v_max_i32_e32 v173, v179, v181
	v_min_i32_e32 v181, v179, v181
	v_max_i32_e32 v178, v173, v172
	v_min_i32_e32 v172, v173, v172
	v_max_i32_e32 v180, v182, v183
	v_min_i32_e32 v183, v182, v183
	v_max_i32_e32 v162, v184, v185
	v_min_i32_e32 v185, v184, v185
	v_max_i32_e32 v179, v180, v162
	v_min_i32_e32 v162, v180, v162
	v_max_i32_e32 v173, v183, v185
	v_min_i32_e32 v185, v183, v185
	v_max_i32_e32 v182, v173, v162
	v_min_i32_e32 v162, v173, v162
	v_max_i32_e32 v184, v169, v179
	v_min_i32_e32 v179, v169, v179
	v_max_i32_e32 v180, v172, v162
	v_min_i32_e32 v162, v172, v162
	v_max_i32_e32 v183, v180, v179
	v_min_i32_e32 v179, v180, v179
	v_max_i32_e32 v173, v178, v182
	v_min_i32_e32 v182, v178, v182
	v_max_i32_e32 v169, v181, v185
	v_min_i32_e32 v185, v181, v185
	v_max_i32_e32 v172, v169, v182
	v_min_i32_e32 v182, v169, v182
	v_max_i32_e32 v180, v173, v183
	v_min_i32_e32 v183, v173, v183
	v_max_i32_e32 v178, v172, v179
	v_min_i32_e32 v179, v172, v179
	v_max_i32_e32 v181, v182, v162
	v_min_i32_e32 v162, v182, v162
	v_max_i32_e32 v169, v186, v187
	v_min_i32_e32 v187, v186, v187
	v_max_i32_e32 v173, v188, v189
	v_min_i32_e32 v189, v188, v189
	v_max_i32_e32 v172, v169, v173
	v_min_i32_e32 v173, v169, v173
	v_max_i32_e32 v182, v187, v189
	v_min_i32_e32 v189, v187, v189
	v_max_i32_e32 v186, v182, v173
	v_min_i32_e32 v173, v182, v173
	v_max_i32_e32 v188, v190, v191
	v_min_i32_e32 v191, v190, v191
; #define LAS __attribute__((address_space(3)))
; #define TOPK_INSERT(arr, xx) do { int _x = (xx); _Pragma("unroll") for (int _j = 0; _j < 16; ++_j) { const int _hi = max(arr[_j], _x); _x = min(arr[_j], _x); arr[_j] = _hi; } } while (0)
; DI void routing_block(LAS unsigned char* lds, const bf16* q, const bf16* skb, int* experts, float* pgates, int tb) {
;     ...
;             LAS int* row = sc + (tid >> 1) * RT_PITCH; const int hf = tid & 1;
; #pragma unroll 8
;             for (int k = 0; k < 64; ++k) { const int x = row[64 * hf + k]; TOPK_INSERT(a, x); }
	v_max_i32_e32 v169, v192, v193
	v_min_i32_e32 v193, v192, v193
	v_max_i32_e32 v187, v188, v169
	v_min_i32_e32 v169, v188, v169
	v_max_i32_e32 v182, v191, v193
	v_min_i32_e32 v193, v191, v193
	v_max_i32_e32 v190, v182, v169
	v_min_i32_e32 v169, v182, v169
	v_max_i32_e32 v192, v172, v187
	v_min_i32_e32 v187, v172, v187
	v_max_i32_e32 v188, v173, v169
	v_min_i32_e32 v169, v173, v169
	v_max_i32_e32 v191, v188, v187
	v_min_i32_e32 v187, v188, v187
	v_max_i32_e32 v182, v186, v190
	v_min_i32_e32 v190, v186, v190
	v_max_i32_e32 v172, v189, v193
	v_min_i32_e32 v193, v189, v193
	v_max_i32_e32 v173, v172, v190
	v_min_i32_e32 v190, v172, v190
	v_max_i32_e32 v188, v182, v191
	v_min_i32_e32 v191, v182, v191
	v_max_i32_e32 v186, v173, v187
	v_min_i32_e32 v187, v173, v187
	v_max_i32_e32 v189, v190, v169
	v_min_i32_e32 v169, v190, v169
	v_max_i32_e32 v172, v184, v192
	v_min_i32_e32 v192, v184, v192
	v_max_i32_e32 v182, v179, v187
	v_min_i32_e32 v187, v179, v187
	v_max_i32_e32 v173, v182, v192
	v_min_i32_e32 v192, v182, v192
	v_max_i32_e32 v190, v183, v191
	v_min_i32_e32 v191, v183, v191
	v_max_i32_e32 v184, v162, v169
	v_min_i32_e32 v169, v162, v169
	v_max_i32_e32 v179, v184, v191
	v_min_i32_e32 v191, v184, v191
	v_max_i32_e32 v182, v190, v173
	v_min_i32_e32 v173, v190, v173
	v_max_i32_e32 v183, v179, v192
	v_min_i32_e32 v192, v179, v192
	v_max_i32_e32 v162, v191, v187
	v_min_i32_e32 v187, v191, v187
	v_max_i32_e32 v184, v180, v188
	v_min_i32_e32 v188, v180, v188
	v_max_i32_e32 v190, v181, v189
	v_min_i32_e32 v189, v181, v189
	v_max_i32_e32 v179, v190, v188
	v_min_i32_e32 v188, v190, v188
	v_max_i32_e32 v191, v178, v186
	v_min_i32_e32 v186, v178, v186
	v_max_i32_e32 v180, v185, v193
	v_min_i32_e32 v193, v185, v193
	v_max_i32_e32 v181, v180, v186
	v_min_i32_e32 v186, v180, v186
	v_max_i32_e32 v190, v191, v179
	v_min_i32_e32 v179, v191, v179
	v_max_i32_e32 v178, v181, v188
	v_min_i32_e32 v188, v181, v188
	v_max_i32_e32 v185, v186, v189
	v_min_i32_e32 v189, v186, v189
	v_max_i32_e32 v180, v184, v182
	v_min_i32_e32 v182, v184, v182
	v_max_i32_e32 v191, v190, v173
	v_min_i32_e32 v173, v190, v173
	v_max_i32_e32 v181, v179, v183
	v_min_i32_e32 v183, v179, v183
	v_max_i32_e32 v186, v178, v192
	v_min_i32_e32 v192, v178, v192
	v_max_i32_e32 v184, v188, v162
	v_min_i32_e32 v162, v188, v162
	v_max_i32_e32 v190, v185, v187
	v_min_i32_e32 v187, v185, v187
	v_max_i32_e32 v179, v189, v169
	v_min_i32_e32 v169, v189, v169
	v_max_i32_e32 v178, v194, v195
	v_min_i32_e32 v195, v194, v195
	v_max_i32_e32 v188, v196, v197
	v_min_i32_e32 v197, v196, v197
	v_max_i32_e32 v185, v178, v188
	v_min_i32_e32 v188, v178, v188
	v_max_i32_e32 v189, v195, v197
	v_min_i32_e32 v197, v195, v197
	v_max_i32_e32 v194, v189, v188
	v_min_i32_e32 v188, v189, v188
	v_max_i32_e32 v196, v198, v199
	v_min_i32_e32 v199, v198, v199
	v_max_i32_e32 v178, v200, v201
	v_min_i32_e32 v201, v200, v201
	v_max_i32_e32 v195, v196, v178
	v_min_i32_e32 v178, v196, v178
	v_max_i32_e32 v189, v199, v201
	v_min_i32_e32 v201, v199, v201
	v_max_i32_e32 v198, v189, v178
	v_min_i32_e32 v178, v189, v178
	v_max_i32_e32 v200, v185, v195
	v_min_i32_e32 v195, v185, v195
	v_max_i32_e32 v196, v188, v178
	v_min_i32_e32 v178, v188, v178
	v_max_i32_e32 v199, v196, v195
	v_min_i32_e32 v195, v196, v195
	v_max_i32_e32 v189, v194, v198
	v_min_i32_e32 v198, v194, v198
	v_max_i32_e32 v185, v197, v201
	v_min_i32_e32 v201, v197, v201
	v_max_i32_e32 v188, v185, v198
	v_min_i32_e32 v198, v185, v198
	v_max_i32_e32 v196, v189, v199
	v_min_i32_e32 v199, v189, v199
	v_max_i32_e32 v194, v188, v195
	v_min_i32_e32 v195, v188, v195
	v_max_i32_e32 v197, v198, v178
	v_min_i32_e32 v178, v198, v178
	v_max_i32_e32 v185, v202, v203
	v_min_i32_e32 v203, v202, v203
	v_max_i32_e32 v189, v204, v205
	v_min_i32_e32 v205, v204, v205
	v_max_i32_e32 v188, v185, v189
	v_min_i32_e32 v189, v185, v189
	v_max_i32_e32 v198, v203, v205
	v_min_i32_e32 v205, v203, v205
	v_max_i32_e32 v202, v198, v189
	v_min_i32_e32 v189, v198, v189
	v_max_i32_e32 v204, v206, v207
	v_min_i32_e32 v207, v206, v207
	v_max_i32_e32 v185, v208, v209
	v_min_i32_e32 v209, v208, v209
	v_max_i32_e32 v203, v204, v185
	v_min_i32_e32 v185, v204, v185
	v_max_i32_e32 v198, v207, v209
	v_min_i32_e32 v209, v207, v209
	v_max_i32_e32 v206, v198, v185
	v_min_i32_e32 v185, v198, v185
	v_max_i32_e32 v208, v188, v203
	v_min_i32_e32 v203, v188, v203
	v_max_i32_e32 v204, v189, v185
	v_min_i32_e32 v185, v189, v185
	v_max_i32_e32 v207, v204, v203
	v_min_i32_e32 v203, v204, v203
	v_max_i32_e32 v198, v202, v206
	v_min_i32_e32 v206, v202, v206
	v_max_i32_e32 v188, v205, v209
	v_min_i32_e32 v209, v205, v209
	v_max_i32_e32 v189, v188, v206
	v_min_i32_e32 v206, v188, v206
	v_max_i32_e32 v204, v198, v207
	v_min_i32_e32 v207, v198, v207
	v_max_i32_e32 v202, v189, v203
	v_min_i32_e32 v203, v189, v203
	v_max_i32_e32 v205, v206, v185
	v_min_i32_e32 v185, v206, v185
	v_max_i32_e32 v188, v200, v208
	v_min_i32_e32 v208, v200, v208
	v_max_i32_e32 v198, v195, v203
	v_min_i32_e32 v203, v195, v203
	v_max_i32_e32 v189, v198, v208
	v_min_i32_e32 v208, v198, v208
	v_max_i32_e32 v206, v199, v207
	v_min_i32_e32 v207, v199, v207
	v_max_i32_e32 v200, v178, v185
	v_min_i32_e32 v185, v178, v185
	v_max_i32_e32 v195, v200, v207
	v_min_i32_e32 v207, v200, v207
	v_max_i32_e32 v198, v206, v189
	v_min_i32_e32 v189, v206, v189
	v_max_i32_e32 v199, v195, v208
	v_min_i32_e32 v208, v195, v208
	v_max_i32_e32 v178, v207, v203
	v_min_i32_e32 v203, v207, v203
	v_max_i32_e32 v200, v196, v204
	v_min_i32_e32 v204, v196, v204
	v_max_i32_e32 v206, v197, v205
	v_min_i32_e32 v205, v197, v205
	v_max_i32_e32 v195, v206, v204
	v_min_i32_e32 v204, v206, v204
; #define LAS __attribute__((address_space(3)))
; #define TOPK_INSERT(arr, xx) do { int _x = (xx); _Pragma("unroll") for (int _j = 0; _j < 16; ++_j) { const int _hi = max(arr[_j], _x); _x = min(arr[_j], _x); arr[_j] = _hi; } } while (0)
; DI void routing_block(LAS unsigned char* lds, const bf16* q, const bf16* skb, int* experts, float* pgates, int tb) {
;     ...
;             LAS int* row = sc + (tid >> 1) * RT_PITCH; const int hf = tid & 1;
; #pragma unroll 8
;             for (int k = 0; k < 64; ++k) { const int x = row[64 * hf + k]; TOPK_INSERT(a, x); }
	v_max_i32_e32 v207, v194, v202
	v_min_i32_e32 v202, v194, v202
	v_max_i32_e32 v196, v201, v209
	v_min_i32_e32 v209, v201, v209
	v_max_i32_e32 v197, v196, v202
	v_min_i32_e32 v202, v196, v202
	v_max_i32_e32 v206, v207, v195
	v_min_i32_e32 v195, v207, v195
	v_max_i32_e32 v194, v197, v204
	v_min_i32_e32 v204, v197, v204
	v_max_i32_e32 v201, v202, v205
	v_min_i32_e32 v205, v202, v205
	v_max_i32_e32 v196, v200, v198
	v_min_i32_e32 v198, v200, v198
	v_max_i32_e32 v207, v206, v189
	v_min_i32_e32 v189, v206, v189
	v_max_i32_e32 v197, v195, v199
	v_min_i32_e32 v199, v195, v199
	v_max_i32_e32 v202, v194, v208
	v_min_i32_e32 v208, v194, v208
	v_max_i32_e32 v200, v204, v178
	v_min_i32_e32 v178, v204, v178
	v_max_i32_e32 v206, v201, v203
	v_min_i32_e32 v203, v201, v203
	v_max_i32_e32 v195, v205, v185
	v_min_i32_e32 v185, v205, v185
	v_max_i32_e32 v19, v19, v177
	v_max_i32_e32 v148, v148, v153
	v_max_i32_e32 v150, v150, v163
	v_max_i32_e32 v159, v159, v171
	v_max_i32_e32 v21, v21, v174
	v_max_i32_e32 v149, v149, v146
	v_max_i32_e32 v151, v151, v168
	v_max_i32_e32 v154, v154, v176
	v_max_i32_e32 v160, v160, v170
	v_max_i32_e32 v152, v152, v167
	v_max_i32_e32 v18, v18, v165
	v_max_i32_e32 v158, v158, v157
	v_max_i32_e32 v155, v155, v175
	v_max_i32_e32 v147, v147, v166
	v_max_i32_e32 v20, v20, v164
	v_max_i32_e32 v161, v161, v156
	v_max_i32_e32 v194, v19, v160
	v_min_i32_e32 v160, v19, v160
	v_max_i32_e32 v204, v148, v152
	v_min_i32_e32 v152, v148, v152
	v_max_i32_e32 v201, v150, v18
	v_min_i32_e32 v18, v150, v18
	v_max_i32_e32 v205, v159, v158
	v_min_i32_e32 v158, v159, v158
	v_max_i32_e32 v156, v21, v155
	v_min_i32_e32 v155, v21, v155
	v_max_i32_e32 v164, v149, v147
	v_min_i32_e32 v147, v149, v147
	v_max_i32_e32 v166, v151, v20
	v_min_i32_e32 v20, v151, v20
	v_max_i32_e32 v175, v154, v161
	v_min_i32_e32 v161, v154, v161
	v_max_i32_e32 v157, v194, v156
	v_min_i32_e32 v156, v194, v156
	v_max_i32_e32 v165, v204, v164
	v_min_i32_e32 v164, v204, v164
	v_max_i32_e32 v167, v201, v166
	v_min_i32_e32 v166, v201, v166
	v_max_i32_e32 v170, v205, v175
	v_min_i32_e32 v175, v205, v175
	v_max_i32_e32 v176, v160, v155
	v_min_i32_e32 v155, v160, v155
	v_max_i32_e32 v168, v152, v147
	v_min_i32_e32 v147, v152, v147
	v_max_i32_e32 v146, v18, v20
	v_min_i32_e32 v20, v18, v20
	v_max_i32_e32 v174, v158, v161
	v_min_i32_e32 v161, v158, v161
	v_max_i32_e32 v171, v157, v167
	v_min_i32_e32 v167, v157, v167
	v_max_i32_e32 v163, v165, v170
	v_min_i32_e32 v170, v165, v170
	v_max_i32_e32 v153, v156, v166
	v_min_i32_e32 v166, v156, v166
	v_max_i32_e32 v177, v164, v175
	v_min_i32_e32 v175, v164, v175
	v_max_i32_e32 v19, v176, v146
	v_min_i32_e32 v146, v176, v146
	v_max_i32_e32 v148, v168, v174
	v_min_i32_e32 v174, v168, v174
	v_max_i32_e32 v150, v155, v20
	v_min_i32_e32 v20, v155, v20
	v_max_i32_e32 v159, v147, v161
	v_min_i32_e32 v161, v147, v161
	v_max_i32_e32 v21, v171, v163
	v_min_i32_e32 v163, v171, v163
	v_max_i32_e32 v149, v167, v170
	v_min_i32_e32 v170, v167, v170
	v_max_i32_e32 v151, v153, v177
	v_min_i32_e32 v177, v153, v177
	v_max_i32_e32 v154, v166, v175
	v_min_i32_e32 v175, v166, v175
	v_max_i32_e32 v194, v19, v148
	v_min_i32_e32 v148, v19, v148
	v_max_i32_e32 v204, v146, v174
	v_min_i32_e32 v174, v146, v174
	v_max_i32_e32 v201, v150, v159
	v_min_i32_e32 v159, v150, v159
	v_max_i32_e32 v205, v20, v161
	v_min_i32_e32 v161, v20, v161
	v_max_i32_e32 v172, v172, v209
	v_max_i32_e32 v180, v180, v185
	v_max_i32_e32 v182, v182, v195
	v_max_i32_e32 v191, v191, v203
	v_max_i32_e32 v173, v173, v206
	v_max_i32_e32 v181, v181, v178
	v_max_i32_e32 v183, v183, v200
	v_max_i32_e32 v186, v186, v208
	v_max_i32_e32 v192, v192, v202
	v_max_i32_e32 v184, v184, v199
	v_max_i32_e32 v162, v162, v197
	v_max_i32_e32 v190, v190, v189
	v_max_i32_e32 v187, v187, v207
	v_max_i32_e32 v179, v179, v198
	v_max_i32_e32 v169, v169, v196
	v_max_i32_e32 v193, v193, v188
	v_max_i32_e32 v160, v172, v192
	v_min_i32_e32 v192, v172, v192
	v_max_i32_e32 v152, v180, v184
	v_min_i32_e32 v184, v180, v184
	v_max_i32_e32 v18, v182, v162
	v_min_i32_e32 v162, v182, v162
	v_max_i32_e32 v158, v191, v190
	v_min_i32_e32 v190, v191, v190
	v_max_i32_e32 v157, v173, v187
	v_min_i32_e32 v187, v173, v187
	v_max_i32_e32 v165, v181, v179
	v_min_i32_e32 v179, v181, v179
	v_max_i32_e32 v156, v183, v169
	v_min_i32_e32 v169, v183, v169
	v_max_i32_e32 v164, v186, v193
	v_min_i32_e32 v193, v186, v193
	v_max_i32_e32 v176, v160, v157
	v_min_i32_e32 v157, v160, v157
	v_max_i32_e32 v168, v152, v165
	v_min_i32_e32 v165, v152, v165
	v_max_i32_e32 v155, v18, v156
	v_min_i32_e32 v156, v18, v156
	v_max_i32_e32 v147, v158, v164
	v_min_i32_e32 v164, v158, v164
	v_max_i32_e32 v171, v192, v187
	v_min_i32_e32 v187, v192, v187
	v_max_i32_e32 v167, v184, v179
	v_min_i32_e32 v179, v184, v179
	v_max_i32_e32 v153, v162, v169
	v_min_i32_e32 v169, v162, v169
	v_max_i32_e32 v166, v190, v193
	v_min_i32_e32 v193, v190, v193
	v_max_i32_e32 v19, v176, v155
	v_min_i32_e32 v155, v176, v155
	v_max_i32_e32 v146, v168, v147
	v_min_i32_e32 v147, v168, v147
	v_max_i32_e32 v150, v157, v156
	v_min_i32_e32 v156, v157, v156
	v_max_i32_e32 v20, v165, v164
	v_min_i32_e32 v164, v165, v164
	v_max_i32_e32 v188, v171, v153
	v_min_i32_e32 v153, v171, v153
	v_max_i32_e32 v196, v167, v166
	v_min_i32_e32 v166, v167, v166
	v_max_i32_e32 v198, v187, v169
	v_min_i32_e32 v169, v187, v169
	v_max_i32_e32 v207, v179, v193
	v_min_i32_e32 v193, v179, v193
	v_max_i32_e32 v189, v19, v146
	v_min_i32_e32 v146, v19, v146
	v_max_i32_e32 v197, v155, v147
	v_min_i32_e32 v147, v155, v147
	v_max_i32_e32 v199, v150, v20
	v_min_i32_e32 v20, v150, v20
	v_max_i32_e32 v202, v156, v164
	v_min_i32_e32 v164, v156, v164
; #define TOPK_INSERT(arr, xx) do { int _x = (xx); _Pragma("unroll") for (int _j = 0; _j < 16; ++_j) { const int _hi = max(arr[_j], _x); _x = min(arr[_j], _x); arr[_j] = _hi; } } while (0)
; DI void routing_block(LAS unsigned char* lds, const bf16* q, const bf16* skb, int* experts, float* pgates, int tb) {
;     ...
;             for (int k = 0; k < 64; ++k) { const int x = row[64 * hf + k]; TOPK_INSERT(a, x); }
;             __syncthreads();
; #pragma unroll
;             for (int j = 0; j < 16; ++j) row[16 * hf + j] = a[j];
;             __syncthreads();
;             if (hf == 0) {
; #pragma unroll
;                 for (int j = 0; j < 16; ++j) { const int x = row[16 + j]; TOPK_INSERT(a, x); }
; #pragma unroll
;                 for (int j = 0; j < 16; ++j) row[j] = a[j];
;             }
	v_max_i32_e32 v208, v188, v196
	v_min_i32_e32 v196, v188, v196
	v_max_i32_e32 v200, v153, v166
	v_min_i32_e32 v166, v153, v166
	v_max_i32_e32 v178, v198, v207
	v_min_i32_e32 v207, v198, v207
	v_max_i32_e32 v206, v169, v193
	v_min_i32_e32 v193, v169, v193
	v_max_i32_e32 v21, v21, v193
	v_max_i32_e32 v163, v163, v206
	v_max_i32_e32 v149, v149, v207
	v_max_i32_e32 v170, v170, v178
	v_max_i32_e32 v151, v151, v166
	v_max_i32_e32 v177, v177, v200
	v_max_i32_e32 v154, v154, v196
	v_max_i32_e32 v175, v175, v208
	v_max_i32_e32 v194, v194, v164
	v_max_i32_e32 v148, v148, v202
	v_max_i32_e32 v204, v204, v20
	v_max_i32_e32 v174, v174, v199
	v_max_i32_e32 v201, v201, v147
	v_max_i32_e32 v159, v159, v197
	v_max_i32_e32 v205, v205, v146
	v_max_i32_e32 v161, v161, v189
	v_max_i32_e32 v203, v21, v194
	v_min_i32_e32 v194, v21, v194
	v_max_i32_e32 v195, v163, v148
	v_min_i32_e32 v148, v163, v148
	v_max_i32_e32 v185, v149, v204
	v_min_i32_e32 v204, v149, v204
	v_max_i32_e32 v209, v170, v174
	v_min_i32_e32 v174, v170, v174
	v_max_i32_e32 v172, v151, v201
	v_min_i32_e32 v201, v151, v201
	v_max_i32_e32 v180, v177, v159
	v_min_i32_e32 v159, v177, v159
	v_max_i32_e32 v182, v154, v205
	v_min_i32_e32 v205, v154, v205
	v_max_i32_e32 v191, v175, v161
	v_min_i32_e32 v161, v175, v161
	v_max_i32_e32 v173, v203, v172
	v_min_i32_e32 v172, v203, v172
	v_max_i32_e32 v181, v195, v180
	v_min_i32_e32 v180, v195, v180
	v_max_i32_e32 v183, v185, v182
	v_min_i32_e32 v182, v185, v182
	v_max_i32_e32 v186, v209, v191
	v_min_i32_e32 v191, v209, v191
	v_max_i32_e32 v160, v194, v201
	v_min_i32_e32 v201, v194, v201
	v_max_i32_e32 v152, v148, v159
	v_min_i32_e32 v159, v148, v159
	v_max_i32_e32 v18, v204, v205
	v_min_i32_e32 v205, v204, v205
	v_max_i32_e32 v158, v174, v161
	v_min_i32_e32 v161, v174, v161
	v_max_i32_e32 v192, v173, v183
	v_min_i32_e32 v183, v173, v183
	v_max_i32_e32 v184, v181, v186
	v_min_i32_e32 v186, v181, v186
	v_max_i32_e32 v162, v172, v182
	v_min_i32_e32 v182, v172, v182
	v_max_i32_e32 v190, v180, v191
	v_min_i32_e32 v191, v180, v191
	v_max_i32_e32 v176, v160, v18
	v_min_i32_e32 v18, v160, v18
	v_max_i32_e32 v168, v152, v158
	v_min_i32_e32 v158, v152, v158
	v_max_i32_e32 v157, v201, v205
	v_min_i32_e32 v205, v201, v205
	v_max_i32_e32 v165, v159, v161
	v_min_i32_e32 v161, v159, v161
	v_max_i32_e32 v171, v192, v184
	v_min_i32_e32 v184, v192, v184
	v_max_i32_e32 v167, v183, v186
	v_min_i32_e32 v186, v183, v186
	v_max_i32_e32 v187, v162, v190
	v_min_i32_e32 v190, v162, v190
	v_max_i32_e32 v179, v182, v191
	v_min_i32_e32 v191, v182, v191
	v_max_i32_e32 v19, v176, v168
	v_min_i32_e32 v168, v176, v168
	v_max_i32_e32 v155, v18, v158
	v_min_i32_e32 v158, v18, v158
	v_max_i32_e32 v150, v157, v165
	v_min_i32_e32 v165, v157, v165
	v_max_i32_e32 v156, v205, v161
	v_min_i32_e32 v161, v205, v161
	s_nop 1
	v_mov_b32_dpp v34, v171 quad_perm:[1,0,3,2] row_mask:0xf bank_mask:0xf
	v_mov_b32_dpp v35, v184 quad_perm:[1,0,3,2] row_mask:0xf bank_mask:0xf
	v_mov_b32_dpp v36, v167 quad_perm:[1,0,3,2] row_mask:0xf bank_mask:0xf
	v_mov_b32_dpp v37, v186 quad_perm:[1,0,3,2] row_mask:0xf bank_mask:0xf
	v_mov_b32_dpp v38, v187 quad_perm:[1,0,3,2] row_mask:0xf bank_mask:0xf
	v_mov_b32_dpp v39, v190 quad_perm:[1,0,3,2] row_mask:0xf bank_mask:0xf
	v_mov_b32_dpp v40, v179 quad_perm:[1,0,3,2] row_mask:0xf bank_mask:0xf
	v_mov_b32_dpp v41, v191 quad_perm:[1,0,3,2] row_mask:0xf bank_mask:0xf
	v_mov_b32_dpp v42, v19 quad_perm:[1,0,3,2] row_mask:0xf bank_mask:0xf
	v_mov_b32_dpp v43, v168 quad_perm:[1,0,3,2] row_mask:0xf bank_mask:0xf
	v_mov_b32_dpp v44, v155 quad_perm:[1,0,3,2] row_mask:0xf bank_mask:0xf
	v_mov_b32_dpp v45, v158 quad_perm:[1,0,3,2] row_mask:0xf bank_mask:0xf
	v_mov_b32_dpp v46, v150 quad_perm:[1,0,3,2] row_mask:0xf bank_mask:0xf
	v_mov_b32_dpp v47, v165 quad_perm:[1,0,3,2] row_mask:0xf bank_mask:0xf
	v_mov_b32_dpp v48, v156 quad_perm:[1,0,3,2] row_mask:0xf bank_mask:0xf
	v_mov_b32_dpp v49, v161 quad_perm:[1,0,3,2] row_mask:0xf bank_mask:0xf
	v_max_i32_e32 v171, v171, v49
	v_max_i32_e32 v184, v184, v48
	v_max_i32_e32 v167, v167, v47
	v_max_i32_e32 v186, v186, v46
	v_max_i32_e32 v187, v187, v45
	v_max_i32_e32 v190, v190, v44
	v_max_i32_e32 v179, v179, v43
	v_max_i32_e32 v191, v191, v42
	v_max_i32_e32 v19, v19, v41
	v_max_i32_e32 v168, v168, v40
	v_max_i32_e32 v155, v155, v39
	v_max_i32_e32 v158, v158, v38
	v_max_i32_e32 v150, v150, v37
	v_max_i32_e32 v165, v165, v36
	v_max_i32_e32 v156, v156, v35
	v_max_i32_e32 v161, v161, v34
	v_max_i32_e32 v188, v171, v19
	v_min_i32_e32 v19, v171, v19
	v_max_i32_e32 v153, v184, v168
	v_min_i32_e32 v168, v184, v168
	v_max_i32_e32 v198, v167, v155
	v_min_i32_e32 v155, v167, v155
	v_max_i32_e32 v169, v186, v158
	v_min_i32_e32 v158, v186, v158
	v_max_i32_e32 v189, v187, v150
	v_min_i32_e32 v150, v187, v150
	v_max_i32_e32 v146, v190, v165
	v_min_i32_e32 v165, v190, v165
	v_max_i32_e32 v197, v179, v156
	v_min_i32_e32 v156, v179, v156
	v_max_i32_e32 v147, v191, v161
	v_min_i32_e32 v161, v191, v161
	v_max_i32_e32 v199, v188, v189
	v_min_i32_e32 v189, v188, v189
	v_max_i32_e32 v20, v153, v146
	v_min_i32_e32 v146, v153, v146
	v_max_i32_e32 v202, v198, v197
	v_min_i32_e32 v197, v198, v197
	v_max_i32_e32 v164, v169, v147
	v_min_i32_e32 v147, v169, v147
	v_max_i32_e32 v208, v19, v150
	v_min_i32_e32 v150, v19, v150
	v_max_i32_e32 v196, v168, v165
	v_min_i32_e32 v165, v168, v165
	v_max_i32_e32 v200, v155, v156
	v_min_i32_e32 v156, v155, v156
	v_max_i32_e32 v166, v158, v161
	v_min_i32_e32 v161, v158, v161
	v_max_i32_e32 v178, v199, v202
	v_min_i32_e32 v202, v199, v202
	v_max_i32_e32 v207, v20, v164
	v_min_i32_e32 v164, v20, v164
	v_max_i32_e32 v206, v189, v197
	v_min_i32_e32 v197, v189, v197
	v_max_i32_e32 v193, v146, v147
	v_min_i32_e32 v147, v146, v147
	v_max_i32_e32 v21, v208, v200
	v_min_i32_e32 v200, v208, v200
	v_max_i32_e32 v163, v196, v166
	v_min_i32_e32 v166, v196, v166
	v_max_i32_e32 v149, v150, v156
	v_min_i32_e32 v156, v150, v156
	v_max_i32_e32 v170, v165, v161
	v_min_i32_e32 v161, v165, v161
	v_max_i32_e32 v151, v178, v207
	v_min_i32_e32 v207, v178, v207
	v_max_i32_e32 v177, v202, v164
	v_min_i32_e32 v164, v202, v164
	v_max_i32_e32 v154, v206, v193
	v_min_i32_e32 v193, v206, v193
	v_max_i32_e32 v175, v197, v147
	v_min_i32_e32 v147, v197, v147
	v_max_i32_e32 v203, v21, v163
	v_min_i32_e32 v163, v21, v163
	v_max_i32_e32 v195, v200, v166
	v_min_i32_e32 v166, v200, v166
	v_max_i32_e32 v185, v149, v170
	v_min_i32_e32 v170, v149, v170
	v_max_i32_e32 v209, v156, v161
	v_min_i32_e32 v161, v156, v161
	s_and_saveexec_b64 s[76:77], s[44:45]
	s_cbranch_execz .LBB0_898
	ds_write2_b32 v119, v151, v207 offset0:0 offset1:1
	ds_write2_b32 v119, v177, v164 offset0:2 offset1:3
	ds_write2_b32 v119, v154, v193 offset0:4 offset1:5
	ds_write2_b32 v119, v175, v147 offset0:6 offset1:7
	ds_write2_b32 v119, v203, v163 offset0:8 offset1:9
	ds_write2_b32 v119, v195, v166 offset0:10 offset1:11
	ds_write2_b32 v119, v185, v170 offset0:12 offset1:13
	ds_write2_b32 v119, v209, v161 offset0:14 offset1:15
